# v035 + Fourier-fold loop handles the thread's four items per trip (16 loads in flight, then four folds and stores)
# baseline (speedup 1.0000x reference)
; __device__ __forceinline__ unsigned pk2(float lo, float hi) { unsigned r; asm("v_cvt_pk_bf16_f32 %0, %1, %2" : "=v"(r) : "v"(lo), "v"(hi)); return r; }
; __device__ __forceinline__ float bf2f(unsigned b) { return __uint_as_float(b << 16); }
; __device__ __forceinline__ float bflo(unsigned w) { return __uint_as_float(w << 16); }
; __device__ __forceinline__ float bfhi(unsigned w) { return __uint_as_float(w & 0xffff0000u); }
; __device__ __forceinline__ void phase_pqfold(const Ptrs& P, int tid_, int vcu, int G) {
;     ...
;     for (size_t i = gt; i < (size_t)2048 * 2048 / 8; i += NGT) { const int row = (int)(i >> 8), k8 = (int)(i & 255) * 8; const bool sinpart = k8 >= 1024; const int s8 = k8 & 1023;
;         const bf16* src = PQ + (size_t)row * 4096 + (sinpart ? 2048 : 0);
;         const v4u f = *(const v4u*)(src + s8); const unsigned fw[4] = {f.x, f.y, f.z, f.w}; float v[8];
; #pragma unroll
;         for (int j = 0; j < 8; ++j) { const int sx = s8 + j; const float a = (j & 1) ? bfhi(fw[j >> 1]) : bflo(fw[j >> 1]); const float r = (sx > 0) ? bf2f(src[2048 - sx]) : 0.f;
;             v[j] = sinpart ? ((sx > 0) ? a - r : bf2f(PQ[(size_t)row * 4096 + 1024])) : a + r; }
;         v4u w; w.x = pk2(v[0], v[1]); w.y = pk2(v[2], v[3]); w.z = pk2(v[4], v[5]); w.w = pk2(v[6], v[7]); ((v4u*)PF)[i] = w; }
.LBB0_693:
	s_mov_b64 s[48:49], exec
	s_lshl_b64 s[50:51], s[28:29], 1
	s_mov_b64 s[4:5], 0x80000
	v_lshl_add_u64 v[20:21], v[6:7], 0, s[24:25]
	v_lshl_add_u64 v[22:23], v[20:21], 0, s[24:25]
	v_lshl_add_u64 v[24:25], v[22:23], 0, s[24:25]
	v_cmp_gt_u64_e64 s[42:43], s[4:5], v[20:21]
	v_cmp_gt_u64_e64 s[44:45], s[4:5], v[22:23]
	v_cmp_gt_u64_e64 s[46:47], s[4:5], v[24:25]
	v_and_b32_e32 v2, 0x7ff000, v8
	v_and_b32_e32 v14, 0x80, v6
	v_lshlrev_b32_e32 v162, 1, v2
	v_and_b32_e32 v15, 0x3f8, v1
	v_lshl_add_u64 v[12:13], s[8:9], 0, v[162:163]
	v_lshlrev_b32_e32 v162, 5, v14
	v_lshl_add_u64 v[10:11], v[12:13], 0, v[162:163]
	v_cmp_ne_u32_e64 s[38:39], 0, v15
	v_cmp_ne_u32_e64 s[40:41], 0, v14
	v_cmp_eq_u32_e32 vcc, 0, v14
	v_lshlrev_b32_e32 v26, 1, v15
	v_mov_b32_e32 v27, 0
	v_xor_b32_e32 v28, 0x3f8, v15
	v_lshlrev_b32_e32 v28, 1, v28
	v_add_u32_e32 v28, 0x80e, v28
	v_mov_b32_e32 v29, 0
	v_sub_u32_e32 v30, 0x7f9, v15
	v_lshlrev_b32_e32 v30, 1, v30
	v_mov_b32_e32 v31, 0
	v_sub_u32_e32 v32, 0x800, v15
	v_lshlrev_b32_e32 v32, 1, v32
	v_mov_b32_e32 v33, 0xfffff800
	v_cndmask_b32_e64 v33, 0, v33, s[40:41]
	v_cndmask_b32_e64 v32, v33, v32, s[38:39]
	v_ashrrev_i32_e32 v33, 31, v32
	s_lshl_b32 s4, s50, 1
	s_add_i32 s5, s4, s50
	v_mov_b32_e32 v34, v10
	v_mov_b32_e32 v35, v11
	v_mov_b32_e32 v162, s50
	v_cndmask_b32_e64 v162, 0, v162, s[42:43]
	v_lshl_add_u64 v[36:37], v[10:11], 0, v[162:163]
	v_mov_b32_e32 v162, s4
	v_cndmask_b32_e64 v162, 0, v162, s[44:45]
	v_lshl_add_u64 v[38:39], v[10:11], 0, v[162:163]
	v_mov_b32_e32 v162, s5
	v_cndmask_b32_e64 v162, 0, v162, s[46:47]
	v_lshl_add_u64 v[40:41], v[10:11], 0, v[162:163]
	v_lshl_add_u64 v[140:141], s[0:1], 0, v[8:9]
	v_lshl_add_u64 v[142:143], v[140:141], 0, s[28:29]
	v_lshl_add_u64 v[144:145], v[142:143], 0, s[28:29]
	v_lshl_add_u64 v[146:147], v[144:145], 0, s[28:29]
	v_lshl_add_u64 v[44:45], v[34:35], 0, v[26:27]
	v_lshl_add_u64 v[46:47], v[34:35], 0, v[28:29]
	v_lshl_add_u64 v[48:49], v[34:35], 0, v[30:31]
	v_lshl_add_u64 v[50:51], v[34:35], 0, v[32:33]
	global_load_dwordx4 v[80:83], v[44:45], off
	global_load_ushort v84, v[46:47], off
	global_load_dwordx3 v[86:88], v[48:49], off
	global_load_ushort v90, v[50:51], off
	v_lshl_add_u64 v[52:53], v[36:37], 0, v[26:27]
	v_lshl_add_u64 v[54:55], v[36:37], 0, v[28:29]
	v_lshl_add_u64 v[56:57], v[36:37], 0, v[30:31]
	v_lshl_add_u64 v[58:59], v[36:37], 0, v[32:33]
	global_load_dwordx4 v[96:99], v[52:53], off
	global_load_ushort v100, v[54:55], off
	global_load_dwordx3 v[102:104], v[56:57], off
	global_load_ushort v106, v[58:59], off
	v_lshl_add_u64 v[60:61], v[38:39], 0, v[26:27]
	v_lshl_add_u64 v[62:63], v[38:39], 0, v[28:29]
	v_lshl_add_u64 v[64:65], v[38:39], 0, v[30:31]
	v_lshl_add_u64 v[66:67], v[38:39], 0, v[32:33]
	global_load_dwordx4 v[112:115], v[60:61], off
	global_load_ushort v116, v[62:63], off
	global_load_dwordx3 v[118:120], v[64:65], off
	global_load_ushort v122, v[66:67], off
	v_lshl_add_u64 v[68:69], v[40:41], 0, v[26:27]
	v_lshl_add_u64 v[70:71], v[40:41], 0, v[28:29]
	v_lshl_add_u64 v[72:73], v[40:41], 0, v[30:31]
	v_lshl_add_u64 v[74:75], v[40:41], 0, v[32:33]
	global_load_dwordx4 v[128:131], v[68:69], off
	global_load_ushort v132, v[70:71], off
	global_load_dwordx3 v[134:136], v[72:73], off
	global_load_ushort v138, v[74:75], off
	s_waitcnt vmcnt(12)
	v_lshlrev_b32_e32 v12, 16, v84
	v_cndmask_b32_e64 v12, -v12, v12, vcc
	v_and_b32_e32 v13, 0xffff0000, v80
	v_add_f32_e32 v13, v12, v13
	v_lshlrev_b32_e32 v17, 16, v80
	v_lshlrev_b32_e32 v16, 16, v90
	v_cndmask_b32_e64 v18, 0, v16, s[38:39]
	v_add_f32_e32 v18, v18, v17
	v_sub_f32_e32 v19, v17, v16
	v_cndmask_b32_e64 v19, v16, v19, s[38:39]
	v_cndmask_b32_e32 v18, v19, v18, vcc
	v_cvt_pk_bf16_f32 v80, v18, v13
	v_and_b32_e32 v12, 0xffff0000, v88
	v_cndmask_b32_e64 v12, -v12, v12, vcc
	v_lshlrev_b32_e32 v13, 16, v81
	v_add_f32_e32 v13, v12, v13
	v_lshlrev_b32_e32 v12, 16, v88
	v_cndmask_b32_e64 v12, -v12, v12, vcc
	v_and_b32_e32 v16, 0xffff0000, v81
	v_add_f32_e32 v16, v12, v16
	v_cvt_pk_bf16_f32 v81, v13, v16
	v_and_b32_e32 v12, 0xffff0000, v87
	v_cndmask_b32_e64 v12, -v12, v12, vcc
	v_lshlrev_b32_e32 v13, 16, v82
	v_add_f32_e32 v13, v12, v13
	v_lshlrev_b32_e32 v12, 16, v87
	v_cndmask_b32_e64 v12, -v12, v12, vcc
	v_and_b32_e32 v16, 0xffff0000, v82
	v_add_f32_e32 v16, v12, v16
	v_cvt_pk_bf16_f32 v82, v13, v16
	v_and_b32_e32 v12, 0xffff0000, v86
	v_cndmask_b32_e64 v12, -v12, v12, vcc
	v_lshlrev_b32_e32 v13, 16, v83
	v_add_f32_e32 v13, v12, v13
	v_lshlrev_b32_e32 v12, 16, v86
	v_cndmask_b32_e64 v12, -v12, v12, vcc
	v_and_b32_e32 v16, 0xffff0000, v83
	v_add_f32_e32 v16, v12, v16
	v_cvt_pk_bf16_f32 v83, v13, v16
	global_store_dwordx4 v[140:141], v[80:83], off
	s_waitcnt vmcnt(8)
; __device__ __forceinline__ unsigned pk2(float lo, float hi) { unsigned r; asm("v_cvt_pk_bf16_f32 %0, %1, %2" : "=v"(r) : "v"(lo), "v"(hi)); return r; }
; __device__ __forceinline__ float bf2f(unsigned b) { return __uint_as_float(b << 16); }
; __device__ __forceinline__ float bflo(unsigned w) { return __uint_as_float(w << 16); }
; __device__ __forceinline__ float bfhi(unsigned w) { return __uint_as_float(w & 0xffff0000u); }
; __device__ __forceinline__ void phase_pqfold(const Ptrs& P, int tid_, int vcu, int G) {
;     ...
;     for (size_t i = gt; i < (size_t)2048 * 2048 / 8; i += NGT) { const int row = (int)(i >> 8), k8 = (int)(i & 255) * 8; const bool sinpart = k8 >= 1024; const int s8 = k8 & 1023;
;         const bf16* src = PQ + (size_t)row * 4096 + (sinpart ? 2048 : 0);
;         const v4u f = *(const v4u*)(src + s8); const unsigned fw[4] = {f.x, f.y, f.z, f.w}; float v[8];
; #pragma unroll
;         for (int j = 0; j < 8; ++j) { const int sx = s8 + j; const float a = (j & 1) ? bfhi(fw[j >> 1]) : bflo(fw[j >> 1]); const float r = (sx > 0) ? bf2f(src[2048 - sx]) : 0.f;
;             v[j] = sinpart ? ((sx > 0) ? a - r : bf2f(PQ[(size_t)row * 4096 + 1024])) : a + r; }
;         v4u w; w.x = pk2(v[0], v[1]); w.y = pk2(v[2], v[3]); w.z = pk2(v[4], v[5]); w.w = pk2(v[6], v[7]); ((v4u*)PF)[i] = w; }
	v_lshlrev_b32_e32 v12, 16, v100
	v_cndmask_b32_e64 v12, -v12, v12, vcc
	v_and_b32_e32 v13, 0xffff0000, v96
	v_add_f32_e32 v13, v12, v13
	v_lshlrev_b32_e32 v17, 16, v96
	v_lshlrev_b32_e32 v16, 16, v106
	v_cndmask_b32_e64 v18, 0, v16, s[38:39]
	v_add_f32_e32 v18, v18, v17
	v_sub_f32_e32 v19, v17, v16
	v_cndmask_b32_e64 v19, v16, v19, s[38:39]
	v_cndmask_b32_e32 v18, v19, v18, vcc
	v_cvt_pk_bf16_f32 v96, v18, v13
	v_and_b32_e32 v12, 0xffff0000, v104
	v_cndmask_b32_e64 v12, -v12, v12, vcc
	v_lshlrev_b32_e32 v13, 16, v97
	v_add_f32_e32 v13, v12, v13
	v_lshlrev_b32_e32 v12, 16, v104
	v_cndmask_b32_e64 v12, -v12, v12, vcc
	v_and_b32_e32 v16, 0xffff0000, v97
	v_add_f32_e32 v16, v12, v16
	v_cvt_pk_bf16_f32 v97, v13, v16
	v_and_b32_e32 v12, 0xffff0000, v103
	v_cndmask_b32_e64 v12, -v12, v12, vcc
	v_lshlrev_b32_e32 v13, 16, v98
	v_add_f32_e32 v13, v12, v13
	v_lshlrev_b32_e32 v12, 16, v103
	v_cndmask_b32_e64 v12, -v12, v12, vcc
	v_and_b32_e32 v16, 0xffff0000, v98
	v_add_f32_e32 v16, v12, v16
	v_cvt_pk_bf16_f32 v98, v13, v16
	v_and_b32_e32 v12, 0xffff0000, v102
	v_cndmask_b32_e64 v12, -v12, v12, vcc
	v_lshlrev_b32_e32 v13, 16, v99
	v_add_f32_e32 v13, v12, v13
	v_lshlrev_b32_e32 v12, 16, v102
	v_cndmask_b32_e64 v12, -v12, v12, vcc
	v_and_b32_e32 v16, 0xffff0000, v99
	v_add_f32_e32 v16, v12, v16
	v_cvt_pk_bf16_f32 v99, v13, v16
	s_and_b64 exec, exec, s[42:43]
	global_store_dwordx4 v[142:143], v[96:99], off
	s_waitcnt vmcnt(4)
	v_lshlrev_b32_e32 v12, 16, v116
	v_cndmask_b32_e64 v12, -v12, v12, vcc
	v_and_b32_e32 v13, 0xffff0000, v112
	v_add_f32_e32 v13, v12, v13
	v_lshlrev_b32_e32 v17, 16, v112
	v_lshlrev_b32_e32 v16, 16, v122
	v_cndmask_b32_e64 v18, 0, v16, s[38:39]
	v_add_f32_e32 v18, v18, v17
	v_sub_f32_e32 v19, v17, v16
	v_cndmask_b32_e64 v19, v16, v19, s[38:39]
	v_cndmask_b32_e32 v18, v19, v18, vcc
	v_cvt_pk_bf16_f32 v112, v18, v13
	v_and_b32_e32 v12, 0xffff0000, v120
	v_cndmask_b32_e64 v12, -v12, v12, vcc
	v_lshlrev_b32_e32 v13, 16, v113
	v_add_f32_e32 v13, v12, v13
	v_lshlrev_b32_e32 v12, 16, v120
	v_cndmask_b32_e64 v12, -v12, v12, vcc
	v_and_b32_e32 v16, 0xffff0000, v113
	v_add_f32_e32 v16, v12, v16
	v_cvt_pk_bf16_f32 v113, v13, v16
	v_and_b32_e32 v12, 0xffff0000, v119
	v_cndmask_b32_e64 v12, -v12, v12, vcc
	v_lshlrev_b32_e32 v13, 16, v114
	v_add_f32_e32 v13, v12, v13
	v_lshlrev_b32_e32 v12, 16, v119
	v_cndmask_b32_e64 v12, -v12, v12, vcc
	v_and_b32_e32 v16, 0xffff0000, v114
	v_add_f32_e32 v16, v12, v16
	v_cvt_pk_bf16_f32 v114, v13, v16
	v_and_b32_e32 v12, 0xffff0000, v118
	v_cndmask_b32_e64 v12, -v12, v12, vcc
	v_lshlrev_b32_e32 v13, 16, v115
	v_add_f32_e32 v13, v12, v13
	v_lshlrev_b32_e32 v12, 16, v118
	v_cndmask_b32_e64 v12, -v12, v12, vcc
	v_and_b32_e32 v16, 0xffff0000, v115
	v_add_f32_e32 v16, v12, v16
	v_cvt_pk_bf16_f32 v115, v13, v16
	s_and_b64 exec, exec, s[44:45]
	global_store_dwordx4 v[144:145], v[112:115], off
	s_waitcnt vmcnt(0)
	v_lshlrev_b32_e32 v12, 16, v132
	v_cndmask_b32_e64 v12, -v12, v12, vcc
	v_and_b32_e32 v13, 0xffff0000, v128
	v_add_f32_e32 v13, v12, v13
	v_lshlrev_b32_e32 v17, 16, v128
	v_lshlrev_b32_e32 v16, 16, v138
	v_cndmask_b32_e64 v18, 0, v16, s[38:39]
	v_add_f32_e32 v18, v18, v17
	v_sub_f32_e32 v19, v17, v16
	v_cndmask_b32_e64 v19, v16, v19, s[38:39]
	v_cndmask_b32_e32 v18, v19, v18, vcc
	v_cvt_pk_bf16_f32 v128, v18, v13
	v_and_b32_e32 v12, 0xffff0000, v136
	v_cndmask_b32_e64 v12, -v12, v12, vcc
	v_lshlrev_b32_e32 v13, 16, v129
	v_add_f32_e32 v13, v12, v13
	v_lshlrev_b32_e32 v12, 16, v136
	v_cndmask_b32_e64 v12, -v12, v12, vcc
	v_and_b32_e32 v16, 0xffff0000, v129
	v_add_f32_e32 v16, v12, v16
	v_cvt_pk_bf16_f32 v129, v13, v16
	v_and_b32_e32 v12, 0xffff0000, v135
	v_cndmask_b32_e64 v12, -v12, v12, vcc
	v_lshlrev_b32_e32 v13, 16, v130
	v_add_f32_e32 v13, v12, v13
	v_lshlrev_b32_e32 v12, 16, v135
	v_cndmask_b32_e64 v12, -v12, v12, vcc
	v_and_b32_e32 v16, 0xffff0000, v130
	v_add_f32_e32 v16, v12, v16
	v_cvt_pk_bf16_f32 v130, v13, v16
	v_and_b32_e32 v12, 0xffff0000, v134
	v_cndmask_b32_e64 v12, -v12, v12, vcc
	v_lshlrev_b32_e32 v13, 16, v131
	v_add_f32_e32 v13, v12, v13
	v_lshlrev_b32_e32 v12, 16, v134
	v_cndmask_b32_e64 v12, -v12, v12, vcc
	v_and_b32_e32 v16, 0xffff0000, v131
	v_add_f32_e32 v16, v12, v16
	v_cvt_pk_bf16_f32 v131, v13, v16
	s_and_b64 exec, exec, s[46:47]
	global_store_dwordx4 v[146:147], v[128:131], off
	s_mov_b64 exec, s[48:49]
	s_lshl_b64 s[4:5], s[24:25], 2
	v_lshl_add_u64 v[6:7], v[6:7], 0, s[4:5]
	s_lshl_b64 s[4:5], s[28:29], 2
	v_lshl_add_u64 v[8:9], v[8:9], 0, s[4:5]
	s_lshl_b32 s4, s36, 2
	v_add_u32_e32 v1, s4, v1
	s_mov_b64 s[4:5], 0x7ffff
	s_nop 0
	v_cmp_lt_u64_e32 vcc, s[4:5], v[6:7]
	s_or_b64 s[12:13], vcc, s[12:13]
	s_andn2_b64 exec, exec, s[12:13]
	s_cbranch_execnz .LBB0_693
